# grid barrier: XCD leader signals the per-XCD generation word before its own L1 invalidate
# speedup vs baseline: 1.0087x; 1.0087x over previous
; __device__ __forceinline__ unsigned xb_ld(unsigned* p)              { return __hip_atomic_load(p, __ATOMIC_RELAXED, __HIP_MEMORY_SCOPE_AGENT); }
; __device__ __forceinline__ unsigned xb_add(unsigned* p, unsigned v) { return __hip_atomic_fetch_add(p, v, __ATOMIC_RELAXED, __HIP_MEMORY_SCOPE_AGENT); }
; #define XB_SPIN(cond, bar) do { unsigned _sp = 0; while (cond) { __builtin_amdgcn_s_sleep(1); \
;     if ((++_sp & 255u) == 0u) { if (xb_ld(&(bar)[XB_TMO])) break; if (_sp > XB_SPIN_CAP) { atomicAdd(&(bar)[XB_TMO], 1u); break; } } } } while (0)
; __device__ __forceinline__ void xcd_barrier(const XcdBarrier& b, bool t0) {
;     ...
;         const unsigned old = xb_add(&bar[XB_XSUB(b.x)], 1u);
;         const unsigned gen = old / nloc;
;         if (old + 1u == (gen + 1u) * nloc) {
;             __builtin_amdgcn_fence(__ATOMIC_RELEASE, "agent");
;             asm volatile("s_waitcnt vmcnt(0)" ::: "memory");
;             const unsigned og = xb_add(&bar[XB_TOP], 1u);
;             const unsigned tg = og / nx;
;             if (og + 1u == (tg + 1u) * nx) xb_add(&bar[XB_TOPGEN], 1u);
;             else XB_SPIN(xb_ld(&bar[XB_TOPGEN]) == tg, bar);
;             __builtin_amdgcn_fence(__ATOMIC_ACQUIRE, "agent");
;             xb_add(&bar[XB_XGEN(b.x)], 1u);
;             asm volatile("s_waitcnt vmcnt(0)" ::: "memory");
.LBB0_176:
	s_or_b64 exec, exec, s[6:7]
	s_add_i32 s6, s26, 0x900
	s_mov_b32 s7, 0
	s_lshl_b64 s[6:7], s[6:7], 2
	s_add_u32 s0, s0, s6
	s_addc_u32 s1, s1, s7
	v_mov_b32_e32 v2, 1
	v_mov_b64_e32 v[0:1], s[0:1]
	s_waitcnt vmcnt(0) lgkmcnt(0)
	flat_atomic_add v[0:1], v2
	buffer_inv sc1
	s_waitcnt vmcnt(0)

; __device__ __forceinline__ unsigned xb_ld(unsigned* p)              { return __hip_atomic_load(p, __ATOMIC_RELAXED, __HIP_MEMORY_SCOPE_AGENT); }
; __device__ __forceinline__ unsigned xb_add(unsigned* p, unsigned v) { return __hip_atomic_fetch_add(p, v, __ATOMIC_RELAXED, __HIP_MEMORY_SCOPE_AGENT); }
; #define XB_SPIN(cond, bar) do { unsigned _sp = 0; while (cond) { __builtin_amdgcn_s_sleep(1); \
;     if ((++_sp & 255u) == 0u) { if (xb_ld(&(bar)[XB_TMO])) break; if (_sp > XB_SPIN_CAP) { atomicAdd(&(bar)[XB_TMO], 1u); break; } } } } while (0)
; __device__ __forceinline__ void xcd_barrier(const XcdBarrier& b, bool t0) {
;     ...
;         const unsigned old = xb_add(&bar[XB_XSUB(b.x)], 1u);
;         const unsigned gen = old / nloc;
;         if (old + 1u == (gen + 1u) * nloc) {
;             __builtin_amdgcn_fence(__ATOMIC_RELEASE, "agent");
;             asm volatile("s_waitcnt vmcnt(0)" ::: "memory");
;             const unsigned og = xb_add(&bar[XB_TOP], 1u);
;             const unsigned tg = og / nx;
;             if (og + 1u == (tg + 1u) * nx) xb_add(&bar[XB_TOPGEN], 1u);
;             else XB_SPIN(xb_ld(&bar[XB_TOPGEN]) == tg, bar);
;             __builtin_amdgcn_fence(__ATOMIC_ACQUIRE, "agent");
;             xb_add(&bar[XB_XGEN(b.x)], 1u);
;             asm volatile("s_waitcnt vmcnt(0)" ::: "memory");
.LBB0_227:
	s_or_b64 exec, exec, s[4:5]
	s_add_i32 s58, s0, 0x900
	s_lshl_b64 s[0:1], s[58:59], 2
	s_add_u32 s0, s2, s0
	s_addc_u32 s1, s3, s1
	v_mov_b64_e32 v[2:3], s[0:1]
	v_mov_b32_e32 v0, 1
	s_waitcnt vmcnt(0) lgkmcnt(0)
	flat_atomic_add v[2:3], v0
	buffer_inv sc1
	s_waitcnt vmcnt(0)

; __device__ __forceinline__ unsigned xb_ld(unsigned* p)              { return __hip_atomic_load(p, __ATOMIC_RELAXED, __HIP_MEMORY_SCOPE_AGENT); }
; __device__ __forceinline__ unsigned xb_add(unsigned* p, unsigned v) { return __hip_atomic_fetch_add(p, v, __ATOMIC_RELAXED, __HIP_MEMORY_SCOPE_AGENT); }
; #define XB_SPIN(cond, bar) do { unsigned _sp = 0; while (cond) { __builtin_amdgcn_s_sleep(1); \
;     if ((++_sp & 255u) == 0u) { if (xb_ld(&(bar)[XB_TMO])) break; if (_sp > XB_SPIN_CAP) { atomicAdd(&(bar)[XB_TMO], 1u); break; } } } } while (0)
; __device__ __forceinline__ void xcd_barrier(const XcdBarrier& b, bool t0) {
;     ...
;         const unsigned old = xb_add(&bar[XB_XSUB(b.x)], 1u);
;         const unsigned gen = old / nloc;
;         if (old + 1u == (gen + 1u) * nloc) {
;             __builtin_amdgcn_fence(__ATOMIC_RELEASE, "agent");
;             asm volatile("s_waitcnt vmcnt(0)" ::: "memory");
;             const unsigned og = xb_add(&bar[XB_TOP], 1u);
;             const unsigned tg = og / nx;
;             if (og + 1u == (tg + 1u) * nx) xb_add(&bar[XB_TOPGEN], 1u);
;             else XB_SPIN(xb_ld(&bar[XB_TOPGEN]) == tg, bar);
;             __builtin_amdgcn_fence(__ATOMIC_ACQUIRE, "agent");
;             xb_add(&bar[XB_XGEN(b.x)], 1u);
;             asm volatile("s_waitcnt vmcnt(0)" ::: "memory");
.LBB0_317:
	s_or_b64 exec, exec, s[6:7]
	s_add_i32 s58, s0, 0x900
	s_lshl_b64 s[0:1], s[58:59], 2
	s_add_u32 s0, s36, s0
	s_addc_u32 s1, s37, s1
	v_mov_b64_e32 v[2:3], s[0:1]
	v_mov_b32_e32 v0, 1
	s_waitcnt vmcnt(0) lgkmcnt(0)
	flat_atomic_add v[2:3], v0
	buffer_inv sc1
	s_waitcnt vmcnt(0)

; __device__ __forceinline__ unsigned xb_ld(unsigned* p)              { return __hip_atomic_load(p, __ATOMIC_RELAXED, __HIP_MEMORY_SCOPE_AGENT); }
; __device__ __forceinline__ unsigned xb_add(unsigned* p, unsigned v) { return __hip_atomic_fetch_add(p, v, __ATOMIC_RELAXED, __HIP_MEMORY_SCOPE_AGENT); }
; #define XB_SPIN(cond, bar) do { unsigned _sp = 0; while (cond) { __builtin_amdgcn_s_sleep(1); \
;     if ((++_sp & 255u) == 0u) { if (xb_ld(&(bar)[XB_TMO])) break; if (_sp > XB_SPIN_CAP) { atomicAdd(&(bar)[XB_TMO], 1u); break; } } } } while (0)
; __device__ __forceinline__ void xcd_barrier(const XcdBarrier& b, bool t0) {
;     ...
;         const unsigned old = xb_add(&bar[XB_XSUB(b.x)], 1u);
;         const unsigned gen = old / nloc;
;         if (old + 1u == (gen + 1u) * nloc) {
;             __builtin_amdgcn_fence(__ATOMIC_RELEASE, "agent");
;             asm volatile("s_waitcnt vmcnt(0)" ::: "memory");
;             const unsigned og = xb_add(&bar[XB_TOP], 1u);
;             const unsigned tg = og / nx;
;             if (og + 1u == (tg + 1u) * nx) xb_add(&bar[XB_TOPGEN], 1u);
;             else XB_SPIN(xb_ld(&bar[XB_TOPGEN]) == tg, bar);
;             __builtin_amdgcn_fence(__ATOMIC_ACQUIRE, "agent");
;             xb_add(&bar[XB_XGEN(b.x)], 1u);
;             asm volatile("s_waitcnt vmcnt(0)" ::: "memory");
.LBB0_758:
	s_or_b64 exec, exec, s[6:7]
	s_add_i32 s58, s0, 0x900
	s_lshl_b64 s[0:1], s[58:59], 2
	s_add_u32 s0, s42, s0
	s_addc_u32 s1, s43, s1
	v_mov_b64_e32 v[2:3], s[0:1]
	v_mov_b32_e32 v0, 1
	s_waitcnt vmcnt(0) lgkmcnt(0)
	flat_atomic_add v[2:3], v0
	buffer_inv sc1
	s_waitcnt vmcnt(0)

; __device__ __forceinline__ unsigned xb_ld(unsigned* p)              { return __hip_atomic_load(p, __ATOMIC_RELAXED, __HIP_MEMORY_SCOPE_AGENT); }
; __device__ __forceinline__ unsigned xb_add(unsigned* p, unsigned v) { return __hip_atomic_fetch_add(p, v, __ATOMIC_RELAXED, __HIP_MEMORY_SCOPE_AGENT); }
; #define XB_SPIN(cond, bar) do { unsigned _sp = 0; while (cond) { __builtin_amdgcn_s_sleep(1); \
;     if ((++_sp & 255u) == 0u) { if (xb_ld(&(bar)[XB_TMO])) break; if (_sp > XB_SPIN_CAP) { atomicAdd(&(bar)[XB_TMO], 1u); break; } } } } while (0)
; __device__ __forceinline__ void xcd_barrier(const XcdBarrier& b, bool t0) {
;     ...
;         const unsigned old = xb_add(&bar[XB_XSUB(b.x)], 1u);
;         const unsigned gen = old / nloc;
;         if (old + 1u == (gen + 1u) * nloc) {
;             __builtin_amdgcn_fence(__ATOMIC_RELEASE, "agent");
;             asm volatile("s_waitcnt vmcnt(0)" ::: "memory");
;             const unsigned og = xb_add(&bar[XB_TOP], 1u);
;             const unsigned tg = og / nx;
;             if (og + 1u == (tg + 1u) * nx) xb_add(&bar[XB_TOPGEN], 1u);
;             else XB_SPIN(xb_ld(&bar[XB_TOPGEN]) == tg, bar);
;             __builtin_amdgcn_fence(__ATOMIC_ACQUIRE, "agent");
;             xb_add(&bar[XB_XGEN(b.x)], 1u);
;             asm volatile("s_waitcnt vmcnt(0)" ::: "memory");
.LBB0_1171:
	s_or_b64 exec, exec, s[6:7]
	s_add_i32 s58, s0, 0x900
	s_lshl_b64 s[0:1], s[58:59], 2
	s_add_u32 s0, s2, s0
	s_addc_u32 s1, s3, s1
	v_mov_b64_e32 v[2:3], s[0:1]
	v_mov_b32_e32 v0, 1
	s_waitcnt vmcnt(0) lgkmcnt(0)
	flat_atomic_add v[2:3], v0
	buffer_inv sc1
	s_waitcnt vmcnt(0)
